# full-tile unit prologue: A(0) through registers, B(1) issued with A(0), counted wait
# speedup vs baseline: 1.0078x; 1.0032x over previous
; #define G_DMA_A(buf, t, i_) __builtin_amdgcn_raw_ptr_buffer_load_lds(ra, (LAS void*)(lds + (buf) * 65536 + a_wu + (i_) * 8192), 16, ao##i_, (unsigned)(t) * 128u, 0, 0)
; #define G_ISSUE_B(t) do { const unsigned so_ = (unsigned)(t) * 64u * ldbB; _Pragma("unroll") for (int i_ = 0; i_ < 8; ++i_) sb[i_] = __builtin_bit_cast(f32x4, __builtin_amdgcn_raw_buffer_load_b128(rb, bo, so_ + (unsigned)i_ * ldbB, 0)); } while (0)
; #define G_RETIRE() asm volatile("s_waitcnt vmcnt(0)" : "+v"(sb[0]), "+v"(sb[1]), "+v"(sb[2]), "+v"(sb[3]), "+v"(sb[4]), "+v"(sb[5]), "+v"(sb[6]), "+v"(sb[7]) :: "memory")
; #define G_WRITE_B(buf) do { LAS unsigned char* d_ = lds + (buf) * 65536; \
;         _Pragma("unroll") for (int j_ = 0; j_ < 4; ++j_) { u32x4 w_; w_.x = cvtpk(sb[0][j_], sb[1][j_]); w_.y = cvtpk(sb[2][j_], sb[3][j_]); w_.z = cvtpk(sb[4][j_], sb[5][j_]); w_.w = cvtpk(sb[6][j_], sb[7][j_]); \
;             *(LAS u32x4*)(d_ + 32768 + T.b_w + ((T.b_rot + 64u * j_) & 255u)) = w_; } } while (0)
; #define G_LDB(dst, buf, ks) do { const LAS unsigned char* s_ = lds + (buf) * 65536 + (ks) * 1024; _Pragma("unroll") for (int n_ = 0; n_ < 4; ++n_) dst[n_] = *(const LAS bf16x8*)(s_ + T.b_r + n_ * 2048); } while (0)
; #define G_LDA(dst, buf, ks, h_) do { const LAS unsigned char* s_ = lds + (buf) * 65536 + (ks) * 1024; _Pragma("unroll") for (int m_ = 0; m_ < 4; ++m_) dst[m_] = *(const LAS bf16x8*)(s_ + T.a_r + ((h_) * 4 + m_) * 2048); } while (0)
; #define G_SB() __builtin_amdgcn_sched_barrier(0)
; #define G_BAR() do { asm volatile("s_waitcnt lgkmcnt(0)" ::: "memory"); __builtin_amdgcn_s_barrier(); asm volatile("" ::: "memory"); } while (0)
; __device__ __forceinline__ void gemm_kloop(f32x4 (&acc)[8][4], LAS unsigned char* lds, const GemmT& T, ...
;     ...
;     for (int t = 0; t < nt; ++t) { const int cur = t & 1; const bool w1 = t + 1 < nt, i2 = t + 2 < nt;
;         G_LDB(Bf0, cur, 0); G_LDA(AtA, cur, 0, 0); G_SB();
;         G_LDA(AtB, cur, 0, 1); if (w1) { G_DMA_A(cur ^ 1, t + 1, 0); G_DMA_A(cur ^ 1, t + 1, 1); G_DMA_A(cur ^ 1, t + 1, 2); G_DMA_A(cur ^ 1, t + 1, 3); } G_MMA(AtA, Bf0, 0); G_SB();
;         G_LDB(Bf1, cur, 1); G_LDA(AtA, cur, 1, 0); G_MMA(AtB, Bf0, 1); G_SB();
;         G_LDA(AtB, cur, 1, 1); if (w1) { G_RETIRE(); G_WRITE_B(cur ^ 1); } if (i2) G_ISSUE_B(t + 2); G_MMA(AtA, Bf1, 0); G_SB();
;         G_MMA(AtB, Bf1, 1); G_SB();
;         G_BAR(); }
.Lmy_d2g_bar:
	s_waitcnt lgkmcnt(0)
	s_barrier
	s_add_i32 s69, s69, 0x80000
	s_add_i32 s68, s68, 0x10000
	s_addk_i32 s70, 0x80
	s_cmp_eq_u32 s69, 0x100e000
	s_cbranch_scc1 .LBB0_1204

; #define G_DMA_A(buf, t, i_) __builtin_amdgcn_raw_ptr_buffer_load_lds(ra, (LAS void*)(lds + (buf) * 65536 + a_wu + (i_) * 8192), 16, ao##i_, (unsigned)(t) * 128u, 0, 0)
; #define G_ISSUE_B(t) do { const unsigned so_ = (unsigned)(t) * 64u * ldbB; _Pragma("unroll") for (int i_ = 0; i_ < 8; ++i_) sb[i_] = __builtin_bit_cast(f32x4, __builtin_amdgcn_raw_buffer_load_b128(rb, bo, so_ + (unsigned)i_ * ldbB, 0)); } while (0)
; #define G_RETIRE() asm volatile("s_waitcnt vmcnt(0)" : "+v"(sb[0]), "+v"(sb[1]), "+v"(sb[2]), "+v"(sb[3]), "+v"(sb[4]), "+v"(sb[5]), "+v"(sb[6]), "+v"(sb[7]) :: "memory")
; #define G_WRITE_B(buf) do { LAS unsigned char* d_ = lds + (buf) * 65536; \
;         _Pragma("unroll") for (int j_ = 0; j_ < 4; ++j_) { u32x4 w_; w_.x = cvtpk(sb[0][j_], sb[1][j_]); w_.y = cvtpk(sb[2][j_], sb[3][j_]); w_.z = cvtpk(sb[4][j_], sb[5][j_]); w_.w = cvtpk(sb[6][j_], sb[7][j_]); \
;             *(LAS u32x4*)(d_ + 32768 + T.b_w + ((T.b_rot + 64u * j_) & 255u)) = w_; } } while (0)
; #define G_BAR() do { asm volatile("s_waitcnt lgkmcnt(0)" ::: "memory"); __builtin_amdgcn_s_barrier(); asm volatile("" ::: "memory"); } while (0)
; #define G_DMA_A(buf, t, i_) __builtin_amdgcn_raw_ptr_buffer_load_lds(ra, (LAS void*)(lds + (buf) * 65536 + a_wu + (i_) * 8192), 16, ao##i_, (unsigned)(t) * 128u, 0, 0)
; #define G_ISSUE_B(t) do { const unsigned so_ = (unsigned)(t) * 64u * ldbB; _Pragma("unroll") for (int i_ = 0; i_ < 8; ++i_) sb[i_] = __builtin_bit_cast(f32x4, __builtin_amdgcn_raw_buffer_load_b128(rb, bo, so_ + (unsigned)i_ * ldbB, 0)); } while (0)
; #define G_RETIRE() asm volatile("s_waitcnt vmcnt(0)" : "+v"(sb[0]), "+v"(sb[1]), "+v"(sb[2]), "+v"(sb[3]), "+v"(sb[4]), "+v"(sb[5]), "+v"(sb[6]), "+v"(sb[7]) :: "memory")
; #define G_WRITE_B(buf) do { LAS unsigned char* d_ = lds + (buf) * 65536; \
;         _Pragma("unroll") for (int j_ = 0; j_ < 4; ++j_) { u32x4 w_; w_.x = cvtpk(sb[0][j_], sb[1][j_]); w_.y = cvtpk(sb[2][j_], sb[3][j_]); w_.z = cvtpk(sb[4][j_], sb[5][j_]); w_.w = cvtpk(sb[6][j_], sb[7][j_]); \
;             *(LAS u32x4*)(d_ + 32768 + T.b_w + ((T.b_rot + 64u * j_) & 255u)) = w_; } } while (0)
; __device__ __forceinline__ void gemm_kloop(f32x4 (&acc)[8][4], LAS unsigned char* lds, const GemmT& T, ...
;     ...
;     G_ISSUE_B(0); G_DMA_A(0, 0, 0); G_DMA_A(0, 0, 1); G_DMA_A(0, 0, 2); G_DMA_A(0, 0, 3); G_RETIRE(); G_WRITE_B(0);
;     if (nt > 1) G_ISSUE_B(1);
;     G_BAR();
.LBB0_1263:
	s_cbranch_execz .LBB0_1267
	v_readfirstlane_b32 s1, v229
	s_and_b32 s1, s1, 0xfffffc00
	s_add_i32 s1, s1, 0
	s_mov_b32 s38, s26
	s_mov_b32 s39, s27
	v_add_u32_e32 v3, v227, v218
	buffer_load_dwordx4 v[40:43], v223, s[36:39], 0 offen
	v_mov_b32_e32 v36, 0
	buffer_load_dwordx4 v[44:47], v222, s[36:39], 0 offen
	s_mov_b32 s3, 0
	buffer_load_dwordx4 v[48:51], v221, s[36:39], 0 offen
	s_mov_b32 s4, 0x10e000
	buffer_load_dwordx4 v[52:55], v224, s[36:39], 0 offen
	buffer_load_dwordx4 v[4:7], v225, s[24:27], s67 offen
	buffer_load_dwordx4 v[8:11], v225, s[24:27], s76 offen
	buffer_load_dwordx4 v[12:15], v225, s[24:27], s77 offen
	buffer_load_dwordx4 v[16:19], v225, s[24:27], s78 offen
	buffer_load_dwordx4 v[20:23], v225, s[24:27], s79 offen
	buffer_load_dwordx4 v[28:31], v225, s[24:27], s80 offen
	buffer_load_dwordx4 v[24:27], v225, s[24:27], s81 offen
	buffer_load_dwordx4 v[32:35], v225, s[24:27], s82 offen
	s_waitcnt vmcnt(8)
	ds_write_b128 v229, v[40:43]
	ds_write_b128 v229, v[44:47] offset:8192
	ds_write_b128 v229, v[48:51] offset:16384
	ds_write_b128 v229, v[52:55] offset:24576
	s_movk_i32 s5, 0x80
	v_cvt_pk_bf16_f32 v56, v114, v126
	v_cvt_pk_bf16_f32 v57, v130, v118
	v_cvt_pk_bf16_f32 v58, v122, v134
	v_cvt_pk_bf16_f32 v59, v142, v146
	ds_write_b128 v228, v[56:59] offset:32768
	v_cvt_pk_bf16_f32 v56, v115, v127
	v_cvt_pk_bf16_f32 v57, v131, v119
	v_cvt_pk_bf16_f32 v58, v123, v135
	v_cvt_pk_bf16_f32 v59, v143, v147
	ds_write_b128 v228, v[56:59] offset:32832
	v_cvt_pk_bf16_f32 v56, v116, v128
	v_cvt_pk_bf16_f32 v57, v132, v120
	v_cvt_pk_bf16_f32 v58, v124, v136
	v_cvt_pk_bf16_f32 v59, v144, v148
	ds_write_b128 v228, v[56:59] offset:32896
	v_cvt_pk_bf16_f32 v56, v117, v129
	v_cvt_pk_bf16_f32 v57, v133, v121
	v_cvt_pk_bf16_f32 v58, v125, v137
	v_cvt_pk_bf16_f32 v59, v145, v149
	ds_write_b128 v3, v[56:59] offset:32768
	s_waitcnt lgkmcnt(0)
	s_barrier
	v_mov_b32_e32 v37, v36
	v_mov_b32_e32 v38, v36
	v_mov_b32_e32 v39, v36
	v_mov_b32_e32 v40, v36
	v_mov_b32_e32 v41, v36
	v_mov_b32_e32 v42, v36
	v_mov_b32_e32 v43, v36
	v_mov_b32_e32 v44, v36
	v_mov_b32_e32 v45, v36
	v_mov_b32_e32 v46, v36
	v_mov_b32_e32 v47, v36
	v_mov_b32_e32 v48, v36
	v_mov_b32_e32 v49, v36
	v_mov_b32_e32 v50, v36
	v_mov_b32_e32 v51, v36
	v_mov_b32_e32 v52, v36
	v_mov_b32_e32 v53, v36
	v_mov_b32_e32 v54, v36
	v_mov_b32_e32 v55, v36
	v_mov_b32_e32 v56, v36
	v_mov_b32_e32 v57, v36
	v_mov_b32_e32 v58, v36
	v_mov_b32_e32 v59, v36
	v_mov_b32_e32 v60, v36
	v_mov_b32_e32 v61, v36
	v_mov_b32_e32 v62, v36
	v_mov_b32_e32 v63, v36
	v_mov_b32_e32 v64, v36
	v_mov_b32_e32 v65, v36
	v_mov_b32_e32 v66, v36
	v_mov_b32_e32 v67, v36
	v_mov_b32_e32 v68, v36
	v_mov_b32_e32 v69, v36
	v_mov_b32_e32 v70, v36
	v_mov_b32_e32 v71, v36
	v_mov_b32_e32 v72, v36
	v_mov_b32_e32 v73, v36
	v_mov_b32_e32 v74, v36
	v_mov_b32_e32 v75, v36
	v_mov_b32_e32 v76, v36
	v_mov_b32_e32 v77, v36
	v_mov_b32_e32 v78, v36
	v_mov_b32_e32 v79, v36
	v_mov_b32_e32 v80, v36
	v_mov_b32_e32 v81, v36
	v_mov_b32_e32 v82, v36
	v_mov_b32_e32 v83, v36
	v_mov_b32_e32 v84, v36
	v_mov_b32_e32 v85, v36
	v_mov_b32_e32 v86, v36
	v_mov_b32_e32 v87, v36
	v_mov_b32_e32 v88, v36
	v_mov_b32_e32 v89, v36
	v_mov_b32_e32 v90, v36
	v_mov_b32_e32 v91, v36
	v_mov_b32_e32 v92, v36
	v_mov_b32_e32 v93, v36
	v_mov_b32_e32 v94, v36
	v_mov_b32_e32 v95, v36
	v_mov_b32_e32 v96, v36
	v_mov_b32_e32 v97, v36
	v_mov_b32_e32 v98, v36
	v_mov_b32_e32 v99, v36
	v_mov_b32_e32 v100, v36
	v_mov_b32_e32 v101, v36
	v_mov_b32_e32 v102, v36
	v_mov_b32_e32 v103, v36
	v_mov_b32_e32 v104, v36
	v_mov_b32_e32 v105, v36
	v_mov_b32_e32 v106, v36
	v_mov_b32_e32 v107, v36
	v_mov_b32_e32 v108, v36
	v_mov_b32_e32 v109, v36
	v_mov_b32_e32 v110, v36
	v_mov_b32_e32 v111, v36
	v_mov_b32_e32 v112, v36
	v_mov_b32_e32 v113, v36
	v_mov_b32_e32 v114, v36
	v_mov_b32_e32 v115, v36
	v_mov_b32_e32 v116, v36
	v_mov_b32_e32 v117, v36
	v_mov_b32_e32 v118, v36
	v_mov_b32_e32 v119, v36
	v_mov_b32_e32 v120, v36
	v_mov_b32_e32 v121, v36
	v_mov_b32_e32 v122, v36
	v_mov_b32_e32 v123, v36
	v_mov_b32_e32 v124, v36
	v_mov_b32_e32 v125, v36
	v_mov_b32_e32 v126, v36
	v_mov_b32_e32 v127, v36
	v_mov_b32_e32 v128, v36
	v_mov_b32_e32 v129, v36
	v_mov_b32_e32 v130, v36
	v_mov_b32_e32 v131, v36
	v_mov_b32_e32 v132, v36
	v_mov_b32_e32 v133, v36
	v_mov_b32_e32 v134, v36
	v_mov_b32_e32 v135, v36
	v_mov_b32_e32 v136, v36
	v_mov_b32_e32 v137, v36
	v_mov_b32_e32 v138, v36
	v_mov_b32_e32 v139, v36
	v_mov_b32_e32 v140, v36
	v_mov_b32_e32 v141, v36
	v_mov_b32_e32 v142, v36
	v_mov_b32_e32 v143, v36
	v_mov_b32_e32 v144, v36
	v_mov_b32_e32 v145, v36
	v_mov_b32_e32 v146, v36
	v_mov_b32_e32 v147, v36
	v_mov_b32_e32 v148, v36
	v_mov_b32_e32 v149, v36
	v_mov_b32_e32 v150, v36
	v_mov_b32_e32 v151, v36
	v_mov_b32_e32 v152, v36
	v_mov_b32_e32 v153, v36
	v_mov_b32_e32 v154, v36
	v_mov_b32_e32 v155, v36
	v_mov_b32_e32 v156, v36
	v_mov_b32_e32 v157, v36
	v_mov_b32_e32 v158, v36
	v_mov_b32_e32 v159, v36
	v_mov_b32_e32 v160, v36
	v_mov_b32_e32 v161, v36
	v_mov_b32_e32 v162, v36
	v_mov_b32_e32 v163, v36

; #define G_DMA_A(buf, t, i_) __builtin_amdgcn_raw_ptr_buffer_load_lds(ra, (LAS void*)(lds + (buf) * 65536 + a_wu + (i_) * 8192), 16, ao##i_, (unsigned)(t) * 128u, 0, 0)
; #define G_ISSUE_B(t) do { const unsigned so_ = (unsigned)(t) * 64u * ldbB; _Pragma("unroll") for (int i_ = 0; i_ < 8; ++i_) sb[i_] = __builtin_bit_cast(f32x4, __builtin_amdgcn_raw_buffer_load_b128(rb, bo, so_ + (unsigned)i_ * ldbB, 0)); } while (0)
; #define G_RETIRE() asm volatile("s_waitcnt vmcnt(0)" : "+v"(sb[0]), "+v"(sb[1]), "+v"(sb[2]), "+v"(sb[3]), "+v"(sb[4]), "+v"(sb[5]), "+v"(sb[6]), "+v"(sb[7]) :: "memory")
; #define G_WRITE_B(buf) do { LAS unsigned char* d_ = lds + (buf) * 65536; \
;         _Pragma("unroll") for (int j_ = 0; j_ < 4; ++j_) { u32x4 w_; w_.x = cvtpk(sb[0][j_], sb[1][j_]); w_.y = cvtpk(sb[2][j_], sb[3][j_]); w_.z = cvtpk(sb[4][j_], sb[5][j_]); w_.w = cvtpk(sb[6][j_], sb[7][j_]); \
;             *(LAS u32x4*)(d_ + 32768 + T.b_w + ((T.b_rot + 64u * j_) & 255u)) = w_; } } while (0)
; #define G_LDB(dst, buf, ks) do { const LAS unsigned char* s_ = lds + (buf) * 65536 + (ks) * 1024; _Pragma("unroll") for (int n_ = 0; n_ < 4; ++n_) dst[n_] = *(const LAS bf16x8*)(s_ + T.b_r + n_ * 2048); } while (0)
; #define G_LDA(dst, buf, ks, h_) do { const LAS unsigned char* s_ = lds + (buf) * 65536 + (ks) * 1024; _Pragma("unroll") for (int m_ = 0; m_ < 4; ++m_) dst[m_] = *(const LAS bf16x8*)(s_ + T.a_r + ((h_) * 4 + m_) * 2048); } while (0)
; #define G_SB() __builtin_amdgcn_sched_barrier(0)
; #define G_BAR() do { asm volatile("s_waitcnt lgkmcnt(0)" ::: "memory"); __builtin_amdgcn_s_barrier(); asm volatile("" ::: "memory"); } while (0)
; __device__ __forceinline__ void gemm_kloop(f32x4 (&acc)[8][4], LAS unsigned char* lds, const GemmT& T, ...
;     ...
;     for (int t = 0; t < nt; ++t) { const int cur = t & 1; const bool w1 = t + 1 < nt, i2 = t + 2 < nt;
;         G_LDB(Bf0, cur, 0); G_LDA(AtA, cur, 0, 0); G_SB();
;         G_LDA(AtB, cur, 0, 1); if (w1) { G_DMA_A(cur ^ 1, t + 1, 0); G_DMA_A(cur ^ 1, t + 1, 1); G_DMA_A(cur ^ 1, t + 1, 2); G_DMA_A(cur ^ 1, t + 1, 3); } G_MMA(AtA, Bf0, 0); G_SB();
;         G_LDB(Bf1, cur, 1); G_LDA(AtA, cur, 1, 0); G_MMA(AtB, Bf0, 1); G_SB();
;         G_LDA(AtB, cur, 1, 1); if (w1) { G_RETIRE(); G_WRITE_B(cur ^ 1); } if (i2) G_ISSUE_B(t + 2); G_MMA(AtA, Bf1, 0); G_SB();
;         G_MMA(AtB, Bf1, 1); G_SB();
;         G_BAR(); }
.Lmy_d2d_bar:
	s_waitcnt lgkmcnt(0)
	s_barrier
	s_add_i32 s72, s72, 0x80000
	s_add_i32 s3, s3, 0x10000
	s_addk_i32 s73, 0x80
	s_cmp_eq_u32 s72, 0x100e000
	s_cbranch_scc1 .LBB0_1515

; #define G_DMA_A(buf, t, i_) __builtin_amdgcn_raw_ptr_buffer_load_lds(ra, (LAS void*)(lds + (buf) * 65536 + a_wu + (i_) * 8192), 16, ao##i_, (unsigned)(t) * 128u, 0, 0)
; #define G_ISSUE_B(t) do { const unsigned so_ = (unsigned)(t) * 64u * ldbB; _Pragma("unroll") for (int i_ = 0; i_ < 8; ++i_) sb[i_] = __builtin_bit_cast(f32x4, __builtin_amdgcn_raw_buffer_load_b128(rb, bo, so_ + (unsigned)i_ * ldbB, 0)); } while (0)
; #define G_RETIRE() asm volatile("s_waitcnt vmcnt(0)" : "+v"(sb[0]), "+v"(sb[1]), "+v"(sb[2]), "+v"(sb[3]), "+v"(sb[4]), "+v"(sb[5]), "+v"(sb[6]), "+v"(sb[7]) :: "memory")
; #define G_WRITE_B(buf) do { LAS unsigned char* d_ = lds + (buf) * 65536; \
;         _Pragma("unroll") for (int j_ = 0; j_ < 4; ++j_) { u32x4 w_; w_.x = cvtpk(sb[0][j_], sb[1][j_]); w_.y = cvtpk(sb[2][j_], sb[3][j_]); w_.z = cvtpk(sb[4][j_], sb[5][j_]); w_.w = cvtpk(sb[6][j_], sb[7][j_]); \
;             *(LAS u32x4*)(d_ + 32768 + T.b_w + ((T.b_rot + 64u * j_) & 255u)) = w_; } } while (0)
; #define G_BAR() do { asm volatile("s_waitcnt lgkmcnt(0)" ::: "memory"); __builtin_amdgcn_s_barrier(); asm volatile("" ::: "memory"); } while (0)
; #define G_DMA_A(buf, t, i_) __builtin_amdgcn_raw_ptr_buffer_load_lds(ra, (LAS void*)(lds + (buf) * 65536 + a_wu + (i_) * 8192), 16, ao##i_, (unsigned)(t) * 128u, 0, 0)
; #define G_ISSUE_B(t) do { const unsigned so_ = (unsigned)(t) * 64u * ldbB; _Pragma("unroll") for (int i_ = 0; i_ < 8; ++i_) sb[i_] = __builtin_bit_cast(f32x4, __builtin_amdgcn_raw_buffer_load_b128(rb, bo, so_ + (unsigned)i_ * ldbB, 0)); } while (0)
; #define G_RETIRE() asm volatile("s_waitcnt vmcnt(0)" : "+v"(sb[0]), "+v"(sb[1]), "+v"(sb[2]), "+v"(sb[3]), "+v"(sb[4]), "+v"(sb[5]), "+v"(sb[6]), "+v"(sb[7]) :: "memory")
; #define G_WRITE_B(buf) do { LAS unsigned char* d_ = lds + (buf) * 65536; \
;         _Pragma("unroll") for (int j_ = 0; j_ < 4; ++j_) { u32x4 w_; w_.x = cvtpk(sb[0][j_], sb[1][j_]); w_.y = cvtpk(sb[2][j_], sb[3][j_]); w_.z = cvtpk(sb[4][j_], sb[5][j_]); w_.w = cvtpk(sb[6][j_], sb[7][j_]); \
;             *(LAS u32x4*)(d_ + 32768 + T.b_w + ((T.b_rot + 64u * j_) & 255u)) = w_; } } while (0)
; __device__ __forceinline__ void gemm_kloop(f32x4 (&acc)[8][4], LAS unsigned char* lds, const GemmT& T, ...
;     ...
;     G_ISSUE_B(0); G_DMA_A(0, 0, 0); G_DMA_A(0, 0, 1); G_DMA_A(0, 0, 2); G_DMA_A(0, 0, 3); G_RETIRE(); G_WRITE_B(0);
;     if (nt > 1) G_ISSUE_B(1);
;     G_BAR();
.LBB0_1574:
	s_cbranch_execz .LBB0_1578
	v_readfirstlane_b32 s1, v230
	s_and_b32 s1, s1, 0xfffffc00
	s_add_i32 s1, s1, 0
	s_mov_b32 s38, s26
	s_mov_b32 s39, s27
	v_add_u32_e32 v3, v228, v221
	buffer_load_dwordx4 v[40:43], v225, s[36:39], 0 offen
	v_mov_b32_e32 v36, 0
	buffer_load_dwordx4 v[44:47], v226, s[36:39], 0 offen
	s_mov_b32 s2, 0
	buffer_load_dwordx4 v[48:51], v224, s[36:39], 0 offen
	s_mov_b32 s3, 0x10e000
	buffer_load_dwordx4 v[52:55], v223, s[36:39], 0 offen
	buffer_load_dwordx4 v[4:7], v222, s[24:27], s67 offen
	buffer_load_dwordx4 v[8:11], v222, s[24:27], s68 offen
	buffer_load_dwordx4 v[12:15], v222, s[24:27], s69 offen
	buffer_load_dwordx4 v[16:19], v222, s[24:27], s70 offen
	buffer_load_dwordx4 v[20:23], v222, s[24:27], s71 offen
	buffer_load_dwordx4 v[28:31], v222, s[24:27], s76 offen
	buffer_load_dwordx4 v[24:27], v222, s[24:27], s77 offen
	buffer_load_dwordx4 v[32:35], v222, s[24:27], s78 offen
	s_waitcnt vmcnt(8)
	ds_write_b128 v230, v[40:43]
	ds_write_b128 v230, v[44:47] offset:8192
	ds_write_b128 v230, v[48:51] offset:16384
	ds_write_b128 v230, v[52:55] offset:24576
	s_movk_i32 s4, 0x80
	v_cvt_pk_bf16_f32 v56, v110, v122
	v_cvt_pk_bf16_f32 v57, v126, v114
	v_cvt_pk_bf16_f32 v58, v118, v130
	v_cvt_pk_bf16_f32 v59, v138, v142
	ds_write_b128 v229, v[56:59] offset:32768
	v_cvt_pk_bf16_f32 v56, v111, v123
	v_cvt_pk_bf16_f32 v57, v127, v115
	v_cvt_pk_bf16_f32 v58, v119, v131
	v_cvt_pk_bf16_f32 v59, v139, v143
	ds_write_b128 v229, v[56:59] offset:32832
	v_cvt_pk_bf16_f32 v56, v112, v124
	v_cvt_pk_bf16_f32 v57, v128, v116
	v_cvt_pk_bf16_f32 v58, v120, v132
	v_cvt_pk_bf16_f32 v59, v140, v144
	ds_write_b128 v229, v[56:59] offset:32896
	v_cvt_pk_bf16_f32 v56, v113, v125
	v_cvt_pk_bf16_f32 v57, v129, v117
	v_cvt_pk_bf16_f32 v58, v121, v133
	v_cvt_pk_bf16_f32 v59, v141, v145
	ds_write_b128 v3, v[56:59] offset:32768
	s_waitcnt lgkmcnt(0)
	s_barrier
	v_mov_b32_e32 v37, v36
	v_mov_b32_e32 v38, v36
	v_mov_b32_e32 v39, v36
	v_mov_b32_e32 v40, v36
	v_mov_b32_e32 v41, v36
	v_mov_b32_e32 v42, v36
	v_mov_b32_e32 v43, v36
	v_mov_b32_e32 v44, v36
	v_mov_b32_e32 v45, v36
	v_mov_b32_e32 v46, v36
	v_mov_b32_e32 v47, v36
	v_mov_b32_e32 v48, v36
	v_mov_b32_e32 v49, v36
	v_mov_b32_e32 v50, v36
	v_mov_b32_e32 v51, v36
	v_mov_b32_e32 v52, v36
	v_mov_b32_e32 v53, v36
	v_mov_b32_e32 v54, v36
	v_mov_b32_e32 v55, v36
	v_mov_b32_e32 v56, v36
	v_mov_b32_e32 v57, v36
	v_mov_b32_e32 v58, v36
	v_mov_b32_e32 v59, v36
	v_mov_b32_e32 v60, v36
	v_mov_b32_e32 v61, v36
	v_mov_b32_e32 v62, v36
	v_mov_b32_e32 v63, v36
	v_mov_b32_e32 v64, v36
	v_mov_b32_e32 v65, v36
	v_mov_b32_e32 v66, v36
	v_mov_b32_e32 v67, v36
	v_mov_b32_e32 v68, v36
	v_mov_b32_e32 v69, v36
	v_mov_b32_e32 v70, v36
	v_mov_b32_e32 v71, v36
	v_mov_b32_e32 v72, v36
	v_mov_b32_e32 v73, v36
	v_mov_b32_e32 v74, v36
	v_mov_b32_e32 v75, v36
	v_mov_b32_e32 v76, v36
	v_mov_b32_e32 v77, v36
	v_mov_b32_e32 v78, v36
	v_mov_b32_e32 v79, v36
	v_mov_b32_e32 v80, v36
	v_mov_b32_e32 v81, v36
	v_mov_b32_e32 v82, v36
	v_mov_b32_e32 v83, v36
	v_mov_b32_e32 v84, v36
	v_mov_b32_e32 v85, v36
	v_mov_b32_e32 v86, v36
	v_mov_b32_e32 v87, v36
	v_mov_b32_e32 v88, v36
	v_mov_b32_e32 v89, v36
	v_mov_b32_e32 v90, v36
	v_mov_b32_e32 v91, v36
	v_mov_b32_e32 v92, v36
	v_mov_b32_e32 v93, v36
	v_mov_b32_e32 v94, v36
	v_mov_b32_e32 v95, v36
	v_mov_b32_e32 v96, v36
	v_mov_b32_e32 v97, v36
	v_mov_b32_e32 v98, v36
	v_mov_b32_e32 v99, v36
	v_mov_b32_e32 v100, v36
	v_mov_b32_e32 v101, v36
	v_mov_b32_e32 v102, v36
	v_mov_b32_e32 v103, v36
	v_mov_b32_e32 v104, v36
	v_mov_b32_e32 v105, v36
	v_mov_b32_e32 v106, v36
	v_mov_b32_e32 v107, v36
	v_mov_b32_e32 v108, v36
	v_mov_b32_e32 v109, v36
	v_mov_b32_e32 v110, v36
	v_mov_b32_e32 v111, v36
	v_mov_b32_e32 v112, v36
	v_mov_b32_e32 v113, v36
	v_mov_b32_e32 v114, v36
	v_mov_b32_e32 v115, v36
	v_mov_b32_e32 v116, v36
	v_mov_b32_e32 v117, v36
	v_mov_b32_e32 v118, v36
	v_mov_b32_e32 v119, v36
	v_mov_b32_e32 v120, v36
	v_mov_b32_e32 v121, v36
	v_mov_b32_e32 v122, v36
	v_mov_b32_e32 v123, v36
	v_mov_b32_e32 v124, v36
	v_mov_b32_e32 v125, v36
	v_mov_b32_e32 v126, v36
	v_mov_b32_e32 v127, v36
	v_mov_b32_e32 v128, v36
	v_mov_b32_e32 v129, v36
	v_mov_b32_e32 v130, v36
	v_mov_b32_e32 v131, v36
	v_mov_b32_e32 v132, v36
	v_mov_b32_e32 v133, v36
	v_mov_b32_e32 v134, v36
	v_mov_b32_e32 v135, v36
	v_mov_b32_e32 v136, v36
	v_mov_b32_e32 v137, v36
	v_mov_b32_e32 v138, v36
	v_mov_b32_e32 v139, v36
	v_mov_b32_e32 v140, v36
	v_mov_b32_e32 v141, v36
	v_mov_b32_e32 v142, v36
	v_mov_b32_e32 v143, v36
	v_mov_b32_e32 v144, v36
	v_mov_b32_e32 v145, v36
	v_mov_b32_e32 v146, v36
	v_mov_b32_e32 v147, v36
	v_mov_b32_e32 v148, v36
	v_mov_b32_e32 v149, v36
	v_mov_b32_e32 v150, v36
	v_mov_b32_e32 v151, v36
	v_mov_b32_e32 v152, v36
	v_mov_b32_e32 v153, v36
	v_mov_b32_e32 v154, v36
	v_mov_b32_e32 v155, v36
	v_mov_b32_e32 v156, v36
	v_mov_b32_e32 v157, v36
	v_mov_b32_e32 v158, v36
	v_mov_b32_e32 v159, v36
	v_mov_b32_e32 v160, v36
	v_mov_b32_e32 v161, v36
	v_mov_b32_e32 v162, v36
	v_mov_b32_e32 v163, v36
